# v033 + routed-down phase reuses the row-block table left in LDS by the gate/up phase (same counters) instead of re-reading the 128 counters and re-scanning
# speedup vs baseline: 1.0196x; 1.0007x over previous
; #define LAS __attribute__((address_space(3)))
; __device__ __forceinline__ int otid() { int t = threadIdx.x; asm volatile("" : "+v"(t)); return t; }
; __device__ __forceinline__ void compute_blkoff(const Ptrs& P, LAS int* tbl, int layer, int tid_) {
;     const int tid = otid(); (void)tid_;
;     __syncthreads();
;     if (tid < 64) {
;         const int lane = tid;
;         const unsigned* cp = (const unsigned*)(P.ws + WS_CTL) + CW_CNT + layer * 256 + 2 * lane;
;         const int n0 = (int)__hip_atomic_load(cp, __ATOMIC_RELAXED, __HIP_MEMORY_SCOPE_AGENT), n1 = (int)__hip_atomic_load(cp + 1, __ATOMIC_RELAXED, __HIP_MEMORY_SCOPE_AGENT);
;         const int b0 = (n0 + 255) >> 8, b1 = (n1 + 255) >> 8; int inc = b0 + b1;
; #pragma unroll
;         for (int off = 1; off < 64; off <<= 1) { const int y = __builtin_amdgcn_ds_bpermute(((lane - off) & 63) << 2, inc); if (lane >= off) inc += y; }
;         const int exc = inc - (b0 + b1);
;         tbl[132 + 2 * lane] = n0; tbl[133 + 2 * lane] = n1; tbl[2 * lane] = exc; tbl[2 * lane + 1] = exc + b0; if (lane == 63) tbl[128] = inc;
;     }
;     __syncthreads();
; }
.LBB0_1317:
	s_andn2_b64 vcc, exec, s[0:1]
	s_cbranch_vccnz .LBB0_1436
	s_mov_b64 s[0:1], s[76:77]
	s_load_dwordx2 s[18:19], s[0:1], 0xd8
	v_mov_b32_e32 v1, v0
	s_waitcnt vmcnt(0) lgkmcnt(0)
	v_cmp_gt_i32_e32 vcc, 64, v1
	s_barrier
	s_and_saveexec_b64 s[0:1], vcc
	s_branch .LBB0_1321
	s_lshl_b32 s16, s86, 8
	s_lshl_b64 s[4:5], s[16:17], 2
	s_add_u32 s4, s18, s4
	v_lshlrev_b32_e32 v2, 1, v1
	s_addc_u32 s5, s19, s5
	v_ashrrev_i32_e32 v3, 31, v2
	v_lshl_add_u64 v[2:3], v[2:3], 2, s[4:5]
	s_mov_b64 s[4:5], 0xea600
	v_lshl_add_u64 v[4:5], v[2:3], 0, s[4:5]
	s_mov_b32 s4, 0xea000
	v_add_co_u32_e32 v2, vcc, s4, v2
	s_movk_i32 s4, 0x80
	s_nop 0
	v_addc_co_u32_e32 v3, vcc, 0, v3, vcc
	global_load_dword v6, v[2:3], off offset:1536 sc1
	global_load_dword v7, v[4:5], off offset:4 sc1
	v_cmp_lt_i32_e32 vcc, 0, v1
	s_waitcnt vmcnt(1)
	v_add_u32_e32 v2, 0xff, v6
	v_ashrrev_i32_e32 v3, 8, v2
	s_waitcnt vmcnt(0)
	v_add_u32_e32 v2, 0xff, v7
	v_ashrrev_i32_e32 v2, 8, v2
	v_add_u32_e32 v4, v2, v3
	v_lshlrev_b32_e32 v2, 2, v1
	v_add_u32_e32 v5, 0xfc, v2
	v_and_b32_e32 v5, 0xfc, v5
	ds_bpermute_b32 v5, v5, v4
	v_add_u32_e32 v8, 0xf8, v2
	v_and_b32_e32 v8, 0xfc, v8
	s_waitcnt lgkmcnt(0)
	v_cndmask_b32_e32 v5, 0, v5, vcc
	v_add_u32_e32 v5, v4, v5
	ds_bpermute_b32 v8, v8, v5
	v_cmp_lt_i32_e32 vcc, 1, v1
	s_waitcnt lgkmcnt(0)
	s_nop 0
	v_cndmask_b32_e32 v8, 0, v8, vcc
	v_add_u32_e32 v5, v5, v8
	v_add_u32_e32 v8, 0xf0, v2
	v_and_b32_e32 v8, 0xfc, v8
	ds_bpermute_b32 v8, v8, v5
	v_cmp_lt_i32_e32 vcc, 3, v1
	s_waitcnt lgkmcnt(0)
	s_nop 0
	v_cndmask_b32_e32 v8, 0, v8, vcc
	v_add_u32_e32 v5, v5, v8
	v_add_u32_e32 v8, 0xe0, v2
	v_and_b32_e32 v8, 0xfc, v8
	ds_bpermute_b32 v8, v8, v5
	v_cmp_lt_i32_e32 vcc, 7, v1
	s_waitcnt lgkmcnt(0)
	s_nop 0
	v_cndmask_b32_e32 v8, 0, v8, vcc
	v_add_u32_e32 v5, v5, v8
	v_add_u32_e32 v8, 0xc0, v2
	v_and_b32_e32 v8, 0xfc, v8
	ds_bpermute_b32 v8, v8, v5
	v_cmp_lt_i32_e32 vcc, 15, v1
	s_waitcnt lgkmcnt(0)
	s_nop 0
	v_cndmask_b32_e32 v8, 0, v8, vcc
	v_add_u32_e32 v5, v5, v8
	v_bfrev_b32_e32 v8, 0.5
	v_bitop3_b32 v2, v2, s4, v8 bitop3:0x6c
	ds_bpermute_b32 v2, v2, v5
	v_cmp_lt_i32_e32 vcc, 31, v1
	s_waitcnt lgkmcnt(0)
	s_nop 0
	v_cndmask_b32_e32 v2, 0, v2, vcc
	v_add_u32_e32 v2, v5, v2
	v_sub_u32_e32 v4, v2, v4
	v_lshl_add_u32 v5, v1, 3, 0
	v_add_u32_e32 v8, 0x20000, v5
	v_add_u32_e32 v5, v4, v3
	v_cmp_eq_u32_e32 vcc, 63, v1
	ds_write2_b64 v8, v[4:5], v[6:7] offset1:66
	s_and_b64 exec, exec, vcc
	s_cbranch_execz .LBB0_1321
	v_readlane_b32 s4, v255, 17
	s_nop 1
	v_mov_b32_e32 v1, s4
	ds_write_b32 v1, v2
